# the three remaining full barrier waits (and the timeout paths of the others) keep two polls in flight and leave the last one undrained
# baseline (speedup 1.0000x reference)
.Lxb_done2_4:
.LBB0_491:
	s_or_b64 exec, exec, s[0:1]
	v_readlane_b32 s0, v235, 16
	v_readlane_b32 s1, v235, 17
	s_lshl_b32 s8, s0, 4
	v_readlane_b32 s0, v235, 0
	v_readlane_b32 s1, v235, 1
	s_mov_b64 s[14:15], s[46:47]
	s_waitcnt lgkmcnt(0)
	v_mov_b32_e32 v0, v186
	s_barrier
	s_load_dwordx2 s[0:1], s[14:15], 0x98
	s_waitcnt vmcnt(14)
	v_ashrrev_i32_e32 v68, 5, v0
	v_readlane_b32 s2, v235, 2
	v_and_b32_e32 v1, -2, v68
	s_lshl_b32 s20, s2, 4
	v_add_u32_e32 v70, s8, v1
	s_movk_i32 s2, 0x2000
	v_readlane_b32 s3, v235, 3
	v_cmp_gt_i32_e32 vcc, s2, v70
	v_writelane_b32 v235, s8, 18
	s_and_saveexec_b64 s[2:3], vcc
	s_cbranch_execz .LBB0_494
	v_bfe_u32 v69, v0, 4, 2
	v_and_b32_e32 v71, 15, v0
	v_lshlrev_b32_e32 v64, 4, v69
	v_mov_b32_e32 v65, 0
	v_lshlrev_b32_e32 v0, 8, v71
	v_mov_b32_e32 v1, v65
	s_waitcnt lgkmcnt(0)
	v_lshl_add_u64 v[66:67], s[0:1], 0, v[64:65]
	v_lshl_add_u64 v[48:49], v[66:67], 0, v[0:1]
	v_add_co_u32_e32 v18, vcc, 0x1adb000, v48
	s_mov_b64 s[8:9], 0x1adb000
	s_nop 0
	v_addc_co_u32_e32 v19, vcc, 0, v49, vcc
	v_add_co_u32_e32 v32, vcc, 0x1adc000, v48
	v_lshl_add_u64 v[16:17], v[48:49], 0, s[8:9]
	s_nop 0
	v_addc_co_u32_e32 v33, vcc, 0, v49, vcc
	v_add_co_u32_e32 v50, vcc, 0x1add000, v48
	global_load_dwordx4 v[0:3], v[16:17], off offset:64
	global_load_dwordx4 v[4:7], v[16:17], off offset:128
	global_load_dwordx4 v[8:11], v[18:19], off
	global_load_dwordx4 v[12:15], v[16:17], off offset:192
	v_addc_co_u32_e32 v51, vcc, 0, v49, vcc
	s_waitcnt vmcnt(17)
	v_add_co_u32_e32 v72, vcc, 0x1ade000, v48
	global_load_dwordx4 v[16:19], v[32:33], off
	global_load_dwordx4 v[20:23], v[32:33], off offset:64
	global_load_dwordx4 v[24:27], v[32:33], off offset:128
	global_load_dwordx4 v[28:31], v[32:33], off offset:192
	v_addc_co_u32_e32 v73, vcc, 0, v49, vcc
	global_load_dwordx4 v[32:35], v[50:51], off
	global_load_dwordx4 v[36:39], v[50:51], off offset:64
	global_load_dwordx4 v[40:43], v[50:51], off offset:128
	global_load_dwordx4 v[44:47], v[50:51], off offset:192
	s_nop 0
	global_load_dwordx4 v[48:51], v[72:73], off
	global_load_dwordx4 v[52:55], v[72:73], off offset:64
	global_load_dwordx4 v[56:59], v[72:73], off offset:128
	global_load_dwordx4 v[60:63], v[72:73], off offset:192
	s_mov_b64 s[10:11], 0x132f3000
	v_lshl_add_u64 v[66:67], v[66:67], 0, s[10:11]
	v_lshrrev_b32_e32 v64, 1, v68
	v_readlane_b32 s10, v235, 16
	v_readlane_b32 s16, v235, 0
	s_add_u32 s8, s0, 0x1971b000
	v_lshlrev_b32_e32 v68, 2, v64
	v_readlane_b32 s11, v235, 17
	v_readlane_b32 s17, v235, 1
	v_readlane_b32 s18, v235, 2
	v_lshlrev_b32_e32 v64, 5, v64
	s_addc_u32 s9, s1, 0
	v_lshlrev_b32_e32 v72, 9, v69
	v_lshl_add_u32 v73, s10, 5, v68
	s_lshl_b32 s12, s18, 5
	v_lshl_add_u32 v74, s10, 8, v64
	s_lshl_b32 s13, s18, 8
	s_mov_b64 s[10:11], 0
	s_movk_i32 s16, 0x60
	s_movk_i32 s17, 0x1fff
	v_readlane_b32 s19, v235, 3
	v_readfirstlane_b32 s100, v186
	s_nop 0
	s_cmp_lg_u32 s100, 0
	s_cbranch_scc1 .Ldfc_w_skip
	s_cmp_eq_u32 s98, 0
	s_cbranch_scc1 .Ldfc_w_skip
	v_readlane_b32 s100, v235, 7
	v_readlane_b32 s101, v235, 8
	v_mov_b32_e32 v236, 0x3400
	v_mov_b32_e32 v239, 0
	s_nop 3

.Lxb_done2_10:
.LBB0_1168:
	s_or_b64 exec, exec, s[0:1]
	v_readlane_b32 s0, v235, 16
	v_readlane_b32 s1, v235, 17
	s_cmpk_lt_i32 s0, 0x200
	v_readlane_b32 s0, v235, 14
	v_readlane_b32 s1, v235, 15
	v_mov_b32_e32 v8, v186
	s_waitcnt lgkmcnt(0)
	s_barrier
	s_nop 0
	v_readfirstlane_b32 s14, v8
	s_cbranch_scc0 .LBB0_1188
	v_lshlrev_b32_e32 v0, 4, v8
	v_add_u32_e32 v1, 0x2000, v0
	v_ashrrev_i32_e32 v2, 31, v1
	v_lshrrev_b32_e32 v2, 22, v2
	v_add_u32_e32 v2, v1, v2
	v_ashrrev_i32_e32 v10, 10, v2
	v_lshlrev_b32_e32 v2, 5, v10
	v_and_b32_e32 v9, 32, v2
	v_mul_i32_i24_e32 v2, 0x400, v10
	v_sub_u32_e32 v1, v1, v2
	v_lshrrev_b32_e32 v2, 4, v1
	v_bitop3_b32 v1, v2, v1, 32 bitop3:0x6c
	v_ashrrev_i32_e32 v2, 31, v1
	v_lshrrev_b32_e32 v2, 26, v2
	v_add_u32_e32 v2, v1, v2
	v_ashrrev_i32_e32 v12, 6, v2
	v_and_b32_e32 v2, 0xc0, v2
	v_lshlrev_b32_e32 v3, 3, v10
	v_sub_u32_e32 v1, v1, v2
	v_mov_b32_e32 v2, 1
	v_and_b32_e32 v3, -16, v3
	v_ashrrev_i16_sdwa v11, v2, sext(v1) dst_sel:DWORD dst_unused:UNUSED_PAD src0_sel:DWORD src1_sel:BYTE_0
	v_add_u32_e32 v3, v12, v3
	s_movk_i32 s16, 0x580
	v_add_u32_sdwa v1, v9, sext(v11) dst_sel:DWORD dst_unused:UNUSED_PAD src0_sel:DWORD src1_sel:WORD_0
	v_mul_lo_u32 v4, v3, s16
	v_add_lshl_u32 v160, v1, v4, 1
	v_ashrrev_i32_e32 v4, 31, v8
	v_lshrrev_b32_e32 v4, 26, v4
	v_add_u32_e32 v4, v8, v4
	v_ashrrev_i32_e32 v14, 6, v4
	v_lshlrev_b32_e32 v4, 5, v14
	v_and_b32_e32 v13, 32, v4
	v_bfe_i32 v4, v8, 27, 1
	v_lshrrev_b32_e32 v4, 22, v4
	v_add_u32_e32 v4, v0, v4
	v_and_b32_e32 v4, 0xfffffc00, v4
	v_sub_u32_e32 v0, v0, v4
	v_lshrrev_b32_e32 v4, 4, v0
	v_bitop3_b32 v4, v4, v0, 32 bitop3:0x6c
	v_ashrrev_i32_e32 v0, 31, v0
	v_lshrrev_b32_e32 v0, 26, v0
	v_add_u32_e32 v0, v4, v0
	v_ashrrev_i32_e32 v16, 6, v0
	v_mul_i32_i24_e32 v0, 64, v16
	v_sub_u32_e32 v0, v4, v0
	v_ashrrev_i16_sdwa v15, v2, sext(v0) dst_sel:DWORD dst_unused:UNUSED_PAD src0_sel:DWORD src1_sel:BYTE_0
	v_lshlrev_b32_e32 v2, 3, v14
	v_and_b32_e32 v2, -16, v2
	s_load_dwordx2 s[6:7], s[0:1], 0x98
	v_add_u32_e32 v2, v16, v2
	v_add_u32_sdwa v0, v13, sext(v15) dst_sel:DWORD dst_unused:UNUSED_PAD src0_sel:DWORD src1_sel:WORD_0
	v_mul_lo_u32 v4, v2, s16
	v_add_lshl_u32 v164, v0, v4, 1
	v_and_b32_e32 v4, 3, v12
	s_mov_b32 s2, 0x1ffffe0
	s_lshl_b32 s0, s47, 3
	v_and_or_b32 v4, v3, s2, v4
	v_lshrrev_b32_e32 v5, 2, v3
	v_lshlrev_b32_e32 v3, 1, v3
	s_or_b32 s59, s0, s46
	v_and_b32_e32 v5, 4, v5
	v_and_b32_e32 v3, 24, v3
	s_waitcnt lgkmcnt(0)
	s_add_u32 s23, s6, 0x11173000
	v_or3_b32 v3, v4, v5, v3
	s_addc_u32 s33, s7, 0
	v_mul_lo_u32 v3, v3, s16
	s_add_u32 s36, s6, 0x7373000
	v_add_lshl_u32 v168, v3, v1, 1
	v_and_b32_e32 v1, 3, v16
	s_addc_u32 s37, s7, 0
	s_ashr_i32 s12, s14, 6
	v_and_or_b32 v1, v2, s2, v1
	v_lshrrev_b32_e32 v3, 2, v2
	v_lshlrev_b32_e32 v2, 1, v2
	s_ashr_i32 s15, s14, 8
	s_lshl_b32 s38, s12, 10
	s_mul_i32 s0, s22, 0xb0000
	v_and_b32_e32 v3, 4, v3
	v_and_b32_e32 v2, 24, v2
	s_mul_hi_i32 s1, s22, 0xb0000
	v_or3_b32 v1, v1, v3, v2
	s_add_u32 s0, s36, s0
	v_mul_lo_u32 v1, v1, s16
	s_addc_u32 s1, s37, s1
	s_add_i32 s39, s38, 0
	v_add_lshl_u32 v170, v1, v0, 1
	v_mov_b32_e32 v188, 0x79797979
	v_mov_b32_e32 v189, 0x7c7c7c7c
	s_add_i32 m0, s39, 0x10000
	s_mul_i32 s5, s59, 0xb0000
	global_load_lds_dwordx4 v170, s[0:1]
	s_add_i32 m0, s39, 0x12000
	s_add_u32 s2, s0, 0x58000
	global_load_lds_dwordx4 v168, s[0:1]
	s_addc_u32 s3, s1, 0
	s_add_i32 m0, s39, 0x14000
	s_mul_hi_i32 s4, s59, 0xb0000
	global_load_lds_dwordx4 v170, s[2:3]
	s_add_i32 m0, s39, 0x16000
	s_add_u32 s28, s23, s5
	global_load_lds_dwordx4 v168, s[2:3]
	s_addc_u32 s29, s33, s4
	v_readfirstlane_b32 s100, v186
	s_nop 0
	s_cmp_lg_u32 s100, 0
	s_cbranch_scc1 .Lgd_p10_skip
	s_cmp_eq_u32 s98, 0
	s_cbranch_scc1 .Lgd_p10_skip
	v_readlane_b32 s100, v235, 7
	v_readlane_b32 s101, v235, 8
	v_mov_b32_e32 v236, 0x3400
	v_mov_b32_e32 v239, 0
	s_nop 3

.Lxb_done2_11:
.LBB0_1241:
	s_or_b64 exec, exec, s[0:1]
	s_waitcnt lgkmcnt(0)
	s_barrier
	v_readlane_b32 s6, v235, 16
	v_readlane_b32 s7, v235, 2
	v_and_b32_e32 v0, 63, v186
	v_lshrrev_b32_e32 v11, 6, v186
	s_load_dwordx2 s[4:5], s[46:47], 0x98
	s_load_dwordx4 s[0:3], s[46:47], 0x88
	v_readfirstlane_b32 s8, v11
	v_lshlrev_b32_e32 v1, 4, v0
	v_lshlrev_b32_e32 v11, 14, v11
	v_add_u32_e32 v11, v11, v1
	v_lshlrev_b32_e32 v2, 5, v0
	v_and_b32_e32 v3, 31, v0
	v_lshlrev_b32_e32 v3, 2, v3
	v_xor_b32_e32 v4, 32, v0
	v_lshlrev_b32_e32 v4, 2, v4
	v_xor_b32_e32 v5, 16, v0
	v_lshlrev_b32_e32 v5, 2, v5
	v_xor_b32_e32 v6, 8, v0
	v_lshlrev_b32_e32 v6, 2, v6
	v_xor_b32_e32 v7, 4, v0
	v_lshlrev_b32_e32 v7, 2, v7
	v_xor_b32_e32 v8, 2, v0
	v_lshlrev_b32_e32 v8, 2, v8
	v_xor_b32_e32 v9, 1, v0
	v_lshlrev_b32_e32 v9, 2, v9
	v_mov_b32_e32 v10, 0x358637bd
	s_lshl_b32 s6, s6, 4
	s_lshl_b32 s8, s8, 1
	s_add_i32 s6, s6, s8
	s_lshl_b32 s7, s7, 4
	s_mov_b32 s23, 0x3a800000
	s_cmp_lt_u32 s6, 0x4000
	s_cbranch_scc0 .Lfin_end
	s_waitcnt lgkmcnt(0)
	s_add_u32 s14, s4, 0x1b73000
	s_addc_u32 s15, s5, 0
	s_add_u32 s16, s4, 0x9f73000
	s_addc_u32 s17, s5, 0
	s_add_u32 s18, s4, 0x15b000
	s_addc_u32 s19, s5, 0
	s_add_u32 s20, s4, 0x5000
	s_addc_u32 s21, s5, 0
	s_add_u32 s34, s20, 0x6000
	s_addc_u32 s35, s21, 0
	global_load_dwordx4 v[12:15], v2, s[0:1]
	global_load_dwordx4 v[16:19], v2, s[0:1] offset:16
	global_load_dwordx4 v[20:23], v2, s[0:1] offset:2048
	global_load_dwordx4 v[24:27], v2, s[0:1] offset:2064
	global_load_dwordx4 v[28:31], v2, s[20:21]
	global_load_dwordx4 v[32:35], v2, s[20:21] offset:16
	global_load_dwordx4 v[36:39], v2, s[20:21] offset:2048
	global_load_dwordx4 v[40:43], v2, s[20:21] offset:2064
	global_load_dwordx4 v[44:47], v2, s[34:35]
	global_load_dwordx4 v[48:51], v2, s[34:35] offset:16
	global_load_dwordx4 v[52:55], v2, s[34:35] offset:2048
	global_load_dwordx4 v[56:59], v2, s[34:35] offset:2064
	s_lshl_b32 s26, s6, 6
	s_add_u32 s24, s18, s26
	s_addc_u32 s25, s19, 0
	global_load_dword v77, v3, s[24:25]
	s_waitcnt vmcnt(0)
	v_readfirstlane_b32 s100, v186
	s_nop 0
	s_cmp_lg_u32 s100, 0
	s_cbranch_scc1 .Lp11_w_skip
	s_cmp_eq_u32 s98, 0
	s_cbranch_scc1 .Lp11_w_skip
	v_readlane_b32 s100, v235, 7
	v_readlane_b32 s101, v235, 8
	v_mov_b32_e32 v236, 0x3400
	v_mov_b32_e32 v239, 0
	s_nop 3
